# v96 + k8 gather phase: the 16 per-thread expert-histogram loads (8 serialized load-pair/vmcnt(0) round trips) issued together from one base with immediate offsets, one wait
# speedup vs baseline: 1.0062x; 1.0009x over previous
.LBB0_1132:
	v_mov_b32_e32 v3, v0
	s_waitcnt vmcnt(0)
	v_ashrrev_i32_e32 v4, 1, v3
	v_and_b32_e32 v5, 31, v3
	v_and_b32_e32 v8, -16, v4
	v_lshl_or_b32 v6, v8, 5, v5
	v_ashrrev_i32_e32 v7, 31, v6
	v_lshl_add_u64 v[6:7], v[6:7], 2, s[48:49]
	s_barrier
	global_load_dword v70, v[6:7], off
	global_load_dword v71, v[6:7], off offset:128
	global_load_dword v72, v[6:7], off offset:256
	global_load_dword v73, v[6:7], off offset:384
	global_load_dword v74, v[6:7], off offset:512
	global_load_dword v75, v[6:7], off offset:640
	global_load_dword v76, v[6:7], off offset:768
	global_load_dword v77, v[6:7], off offset:896
	global_load_dword v78, v[6:7], off offset:1024
	global_load_dword v79, v[6:7], off offset:1152
	global_load_dword v80, v[6:7], off offset:1280
	global_load_dword v81, v[6:7], off offset:1408
	global_load_dword v82, v[6:7], off offset:1536
	global_load_dword v83, v[6:7], off offset:1664
	global_load_dword v84, v[6:7], off offset:1792
	global_load_dword v85, v[6:7], off offset:1920
	v_lshlrev_b32_e32 v5, 2, v5
	v_mov_b32_e32 v10, 0
	s_waitcnt vmcnt(0)
	v_add_u32_e32 v9, v70, v71
	v_add3_u32 v9, v9, v72, v73
	v_add3_u32 v9, v9, v74, v75
	v_add3_u32 v9, v9, v76, v77
	v_add3_u32 v9, v9, v78, v79
	v_add3_u32 v9, v9, v80, v81
	v_add3_u32 v9, v9, v82, v83
	v_add3_u32 v9, v9, v84, v85
	v_or_b32_e32 v11, 0, v8
	v_cmp_gt_i32_e64 s[38:39], s2, v11
	s_nop 1
	v_cndmask_b32_e64 v12, 0, v70, s[38:39]
	v_add_u32_e32 v10, v10, v12
	v_or_b32_e32 v11, 1, v8
	v_cmp_gt_i32_e64 s[38:39], s2, v11
	s_nop 1
	v_cndmask_b32_e64 v12, 0, v71, s[38:39]
	v_add_u32_e32 v10, v10, v12
	v_or_b32_e32 v11, 2, v8
	v_cmp_gt_i32_e64 s[38:39], s2, v11
	s_nop 1
	v_cndmask_b32_e64 v12, 0, v72, s[38:39]
	v_add_u32_e32 v10, v10, v12
	v_or_b32_e32 v11, 3, v8
	v_cmp_gt_i32_e64 s[38:39], s2, v11
	s_nop 1
	v_cndmask_b32_e64 v12, 0, v73, s[38:39]
	v_add_u32_e32 v10, v10, v12
	v_or_b32_e32 v11, 4, v8
	v_cmp_gt_i32_e64 s[38:39], s2, v11
	s_nop 1
	v_cndmask_b32_e64 v12, 0, v74, s[38:39]
	v_add_u32_e32 v10, v10, v12
	v_or_b32_e32 v11, 5, v8
	v_cmp_gt_i32_e64 s[38:39], s2, v11
	s_nop 1
	v_cndmask_b32_e64 v12, 0, v75, s[38:39]
	v_add_u32_e32 v10, v10, v12
	v_or_b32_e32 v11, 6, v8
	v_cmp_gt_i32_e64 s[38:39], s2, v11
	s_nop 1
	v_cndmask_b32_e64 v12, 0, v76, s[38:39]
	v_add_u32_e32 v10, v10, v12
	v_or_b32_e32 v11, 7, v8
	v_cmp_gt_i32_e64 s[38:39], s2, v11
	s_nop 1
	v_cndmask_b32_e64 v12, 0, v77, s[38:39]
	v_add_u32_e32 v10, v10, v12
	v_or_b32_e32 v11, 8, v8
	v_cmp_gt_i32_e64 s[38:39], s2, v11
	s_nop 1
	v_cndmask_b32_e64 v12, 0, v78, s[38:39]
	v_add_u32_e32 v10, v10, v12
	v_or_b32_e32 v11, 9, v8
	v_cmp_gt_i32_e64 s[38:39], s2, v11
	s_nop 1
	v_cndmask_b32_e64 v12, 0, v79, s[38:39]
	v_add_u32_e32 v10, v10, v12
	v_or_b32_e32 v11, 10, v8
	v_cmp_gt_i32_e64 s[38:39], s2, v11
	s_nop 1
	v_cndmask_b32_e64 v12, 0, v80, s[38:39]
	v_add_u32_e32 v10, v10, v12
	v_or_b32_e32 v11, 11, v8
	v_cmp_gt_i32_e64 s[38:39], s2, v11
	s_nop 1
	v_cndmask_b32_e64 v12, 0, v81, s[38:39]
	v_add_u32_e32 v10, v10, v12
	v_or_b32_e32 v11, 12, v8
	v_cmp_gt_i32_e64 s[38:39], s2, v11
	s_nop 1
	v_cndmask_b32_e64 v12, 0, v82, s[38:39]
	v_add_u32_e32 v10, v10, v12
	v_or_b32_e32 v11, 13, v8
	v_cmp_gt_i32_e64 s[38:39], s2, v11
	s_nop 1
	v_cndmask_b32_e64 v12, 0, v83, s[38:39]
	v_add_u32_e32 v10, v10, v12
	v_or_b32_e32 v11, 14, v8
	v_cmp_gt_i32_e64 s[38:39], s2, v11
	s_nop 1
	v_cndmask_b32_e64 v12, 0, v84, s[38:39]
	v_add_u32_e32 v10, v10, v12
	v_or_b32_e32 v11, 15, v8
	v_cmp_gt_i32_e64 s[38:39], s2, v11
	s_nop 1
	v_cndmask_b32_e64 v12, 0, v85, s[38:39]
	v_add_u32_e32 v10, v10, v12
	v_mov_b32_e32 v7, v9
	v_mov_b32_e32 v6, v10
	v_and_b32_e32 v8, 0x3fffffe0, v3
	v_lshl_add_u32 v4, v3, 2, 0
	ds_write_b32 v4, v7
	v_lshlrev_b32_e32 v7, 2, v8
	v_add3_u32 v5, 0, v7, v5
	v_cmp_gt_i32_e64 s[38:39], 32, v3
	ds_write_b32 v5, v6 offset:2048
	s_waitcnt lgkmcnt(0)
	s_barrier
	s_and_saveexec_b64 s[36:37], s[38:39]
	s_cbranch_execz .LBB0_1135
	v_add_u32_e32 v5, 0x800, v4
	ds_read2_b32 v[8:9], v5 offset1:32
	ds_read2_b32 v[6:7], v4 offset1:32
	v_add_u32_e32 v23, 0xc00, v4
	v_add_u32_e32 v22, 0x400, v4
	s_movk_i32 s3, 0xff
	s_waitcnt lgkmcnt(1)
	v_add_u32_e32 v12, v9, v8
	ds_read2_b32 v[8:9], v4 offset0:64 offset1:96
	ds_read2_b32 v[10:11], v5 offset0:64 offset1:96
	s_waitcnt lgkmcnt(0)
	v_add3_u32 v14, v12, v10, v11
	ds_read2_b32 v[10:11], v4 offset0:128 offset1:160
	ds_read2_b32 v[12:13], v5 offset0:128 offset1:160
	s_waitcnt lgkmcnt(0)
	v_add3_u32 v16, v14, v12, v13
	ds_read2_b32 v[12:13], v4 offset0:192 offset1:224
	ds_read2_b32 v[14:15], v5 offset0:192 offset1:224
	s_waitcnt lgkmcnt(0)
	v_add3_u32 v5, v16, v14, v15
	ds_read2_b32 v[16:17], v23 offset1:32
	ds_read2_b32 v[14:15], v22 offset1:32
	s_waitcnt lgkmcnt(1)
	v_add3_u32 v5, v5, v16, v17
	ds_read2_b32 v[16:17], v22 offset0:64 offset1:96
	ds_read2_b32 v[18:19], v23 offset0:64 offset1:96
	s_waitcnt lgkmcnt(0)
	v_add3_u32 v5, v5, v18, v19
	ds_read2_b32 v[18:19], v22 offset0:128 offset1:160
	ds_read2_b32 v[20:21], v23 offset0:128 offset1:160
	s_waitcnt lgkmcnt(0)
	v_add3_u32 v5, v5, v20, v21
	ds_read2_b32 v[20:21], v22 offset0:192 offset1:224
	ds_read2_b32 v[22:23], v23 offset0:192 offset1:224
	s_waitcnt lgkmcnt(0)
	v_add3_u32 v5, v5, v22, v23
	v_add_u32_e32 v22, 0x24e00, v4
	ds_write_b32 v22, v5
	v_add3_u32 v5, v6, v7, v8
	v_add3_u32 v5, v5, v9, v10
	v_add3_u32 v5, v5, v11, v12
	v_add3_u32 v5, v5, v13, v14
	v_add3_u32 v5, v5, v15, v16
	v_add3_u32 v5, v5, v17, v18
	v_add3_u32 v5, v5, v19, v20
	v_add3_u32 v5, v5, v21, s3
	v_ashrrev_i32_e32 v6, 8, v5
	v_and_b32_e32 v5, 64, v249
	v_add_u32_e32 v7, -1, v249
	v_cmp_lt_i32_e64 s[38:39], v7, v5
	v_add_u32_e32 v8, -2, v249
	s_nop 0
	v_cndmask_b32_e64 v7, v7, v249, s[38:39]
	v_lshlrev_b32_e32 v7, 2, v7
	ds_bpermute_b32 v7, v7, v6
	v_cmp_lt_i32_e64 s[38:39], 0, v3
	s_waitcnt lgkmcnt(0)
	s_nop 0
	v_cndmask_b32_e64 v7, 0, v7, s[38:39]
	v_cmp_lt_i32_e64 s[38:39], v8, v5
	v_add_u32_e32 v7, v7, v6
	s_nop 0
	v_cndmask_b32_e64 v8, v8, v249, s[38:39]
	v_lshlrev_b32_e32 v8, 2, v8
	ds_bpermute_b32 v8, v8, v7
	v_cmp_lt_i32_e64 s[38:39], 1, v3
	s_waitcnt lgkmcnt(0)
	s_nop 0
	v_cndmask_b32_e64 v8, 0, v8, s[38:39]
	v_add_u32_e32 v7, v8, v7
	v_add_u32_e32 v8, -4, v249
	v_cmp_lt_i32_e64 s[38:39], v8, v5
	s_nop 1
	v_cndmask_b32_e64 v8, v8, v249, s[38:39]
	v_lshlrev_b32_e32 v8, 2, v8
	ds_bpermute_b32 v8, v8, v7
	v_cmp_lt_i32_e64 s[38:39], 3, v3
	s_waitcnt lgkmcnt(0)
	s_nop 0
	v_cndmask_b32_e64 v8, 0, v8, s[38:39]
	v_add_u32_e32 v7, v8, v7
	v_add_u32_e32 v8, -8, v249
	v_cmp_lt_i32_e64 s[38:39], v8, v5
	s_nop 1
	v_cndmask_b32_e64 v8, v8, v249, s[38:39]
	v_lshlrev_b32_e32 v8, 2, v8
	ds_bpermute_b32 v8, v8, v7
	v_cmp_lt_i32_e64 s[38:39], 7, v3
	s_waitcnt lgkmcnt(0)
	s_nop 0
	v_cndmask_b32_e64 v8, 0, v8, s[38:39]
	v_add_u32_e32 v7, v8, v7
	v_add_u32_e32 v8, -16, v249
	v_cmp_lt_i32_e64 s[38:39], v8, v5
	s_nop 1
	v_cndmask_b32_e64 v5, v8, v249, s[38:39]
	v_lshlrev_b32_e32 v5, 2, v5
	ds_bpermute_b32 v5, v5, v7
	v_cmp_lt_i32_e64 s[38:39], 15, v3
	s_waitcnt lgkmcnt(0)
	s_nop 0
	v_cndmask_b32_e64 v5, 0, v5, s[38:39]
	v_add_u32_e32 v5, v5, v7
	v_sub_u32_e32 v6, v5, v6
	v_add_u32_e32 v7, 0x24840, v4
	v_cmp_eq_u32_e64 s[38:39], 31, v3
	ds_write_b32 v7, v6
	s_and_b64 exec, exec, s[38:39]
	s_cbranch_execz .LBB0_1135
	v_readlane_b32 s3, v254, 33
	v_min_i32_e32 v6, 0xa0, v5
	s_nop 0
	v_mov_b32_e32 v7, s3
	v_readlane_b32 s3, v254, 34
	ds_write_b32 v7, v5
	s_nop 0
	v_mov_b32_e32 v5, s3
	ds_write_b32 v5, v6
